# speedup vs baseline: 1.0149x; 1.0149x over previous
.LBB0_17:
	v_sub_f32_e32 v2, v66, v244
	v_exp_f32_e32 v98, v2
	v_sub_f32_e32 v2, v50, v244
	v_exp_f32_e32 v82, v2
	v_sub_f32_e32 v2, v67, v244
	v_exp_f32_e32 v99, v2
	v_sub_f32_e32 v2, v51, v244
	v_exp_f32_e32 v83, v2
	v_sub_f32_e32 v2, v68, v244
	v_exp_f32_e32 v100, v2
	v_sub_f32_e32 v2, v52, v244
	v_exp_f32_e32 v84, v2
	v_sub_f32_e32 v2, v69, v244
	v_exp_f32_e32 v101, v2
	v_sub_f32_e32 v2, v53, v244
	v_exp_f32_e32 v85, v2
	v_sub_f32_e32 v2, v70, v244
	v_exp_f32_e32 v102, v2
	v_sub_f32_e32 v2, v54, v244
	v_exp_f32_e32 v86, v2
	v_sub_f32_e32 v2, v71, v244
	v_exp_f32_e32 v103, v2
	v_sub_f32_e32 v2, v55, v244
	v_exp_f32_e32 v87, v2
	v_sub_f32_e32 v2, v72, v244
	v_exp_f32_e32 v104, v2
	v_sub_f32_e32 v2, v56, v244
	v_exp_f32_e32 v88, v2
	v_sub_f32_e32 v2, v73, v244
	v_exp_f32_e32 v105, v2
	v_sub_f32_e32 v2, v57, v244
	v_exp_f32_e32 v89, v2
	v_sub_f32_e32 v2, v74, v244
	v_exp_f32_e32 v106, v2
	v_sub_f32_e32 v2, v58, v244
	v_exp_f32_e32 v90, v2
	v_sub_f32_e32 v2, v75, v244
	v_exp_f32_e32 v107, v2
	v_sub_f32_e32 v2, v59, v244
	v_exp_f32_e32 v91, v2
	v_sub_f32_e32 v2, v76, v244
	v_exp_f32_e32 v108, v2
	v_sub_f32_e32 v2, v60, v244
	v_exp_f32_e32 v92, v2
	v_sub_f32_e32 v2, v77, v244
	v_exp_f32_e32 v109, v2
	v_sub_f32_e32 v2, v61, v244
	v_exp_f32_e32 v93, v2
	v_sub_f32_e32 v2, v78, v244
	v_exp_f32_e32 v110, v2
	v_sub_f32_e32 v2, v62, v244
	v_exp_f32_e32 v94, v2
	v_sub_f32_e32 v2, v79, v244
	v_exp_f32_e32 v111, v2
	v_sub_f32_e32 v2, v63, v244
	v_exp_f32_e32 v95, v2
	v_sub_f32_e32 v2, v80, v244
	v_exp_f32_e32 v112, v2
	v_sub_f32_e32 v2, v64, v244
	v_exp_f32_e32 v96, v2
	v_sub_f32_e32 v2, v81, v244
	v_exp_f32_e32 v113, v2
	v_sub_f32_e32 v2, v65, v244
	v_exp_f32_e32 v97, v2
	s_andn2_b64 vcc, exec, s[4:5]
	s_mov_b32 s98, 1
	s_mov_b32 s97, 0
	s_cbranch_vccnz .LBB0_34
	v_mov_b32_e32 v16, v3
	v_mov_b32_e32 v17, v3
	v_mov_b32_e32 v2, v3
	v_mov_b32_e32 v4, v3
	v_mov_b32_e32 v5, v3
	v_mov_b32_e32 v6, v3
	v_mov_b32_e32 v7, v3
	v_mov_b32_e32 v8, v3
	v_mov_b32_e32 v9, v3
	v_mov_b32_e32 v10, v3
	v_mov_b32_e32 v11, v3
	v_mov_b32_e32 v12, v3
	v_mov_b32_e32 v13, v3
	v_mov_b32_e32 v14, v3
	v_mov_b32_e32 v15, v3
	v_mov_b64_e32 v[64:65], v[16:17]
	v_mov_b64_e32 v[80:81], v[16:17]
	s_sub_i32 s66, 0, s82
	s_movk_i32 s77, 0x4000
	v_mov_b32_e32 v243, 0
	s_mov_b32 s98, 2
	s_movk_i32 s99, 0xbb
	v_mov_b32_e32 v160, 0
	v_mov_b32_e32 v161, 0
	v_mov_b32_e32 v156, 0
	v_mov_b32_e32 v157, 0
	v_mov_b32_e32 v152, 0
	v_mov_b32_e32 v153, 0
	v_mov_b32_e32 v148, 0
	v_mov_b32_e32 v149, 0
	v_mov_b64_e32 v[62:63], v[14:15]
	v_mov_b64_e32 v[60:61], v[12:13]
	v_mov_b64_e32 v[58:59], v[10:11]
	v_mov_b64_e32 v[56:57], v[8:9]
	v_mov_b64_e32 v[54:55], v[6:7]
	v_mov_b64_e32 v[52:53], v[4:5]
	v_mov_b64_e32 v[50:51], v[2:3]
	v_mov_b64_e32 v[78:79], v[14:15]
	v_mov_b64_e32 v[76:77], v[12:13]
	v_mov_b64_e32 v[74:75], v[10:11]
	v_mov_b64_e32 v[72:73], v[8:9]
	v_mov_b64_e32 v[70:71], v[6:7]
	v_mov_b64_e32 v[68:69], v[4:5]
	v_mov_b64_e32 v[66:67], v[2:3]
	v_mov_b32_e32 v115, v114
	v_mov_b32_e32 v116, v114
	v_mov_b32_e32 v117, v114
	v_mov_b32_e32 v118, v114
	v_mov_b32_e32 v119, v114
	v_mov_b32_e32 v120, v114
	v_mov_b32_e32 v121, v114
	v_mov_b32_e32 v122, v114
	v_mov_b32_e32 v123, v114
	v_mov_b32_e32 v124, v114
	v_mov_b32_e32 v125, v114
	v_mov_b32_e32 v126, v114
	v_mov_b32_e32 v127, v114
	v_mov_b32_e32 v128, v114
	v_mov_b32_e32 v129, v114
	s_lshl_b32 s4, s76, 12
	s_lshl_b32 s5, s90, 2
	s_add_u32 s4, s4, s5
	s_add_u32 s100, s70, s4
	s_addc_u32 s101, s71, 0
	s_add_u32 s0, s74, s4
	s_addc_u32 s1, s75, 0
	s_sub_u32 s0, s0, 0x40000
	s_subb_u32 s1, s1, 0
	s_add_i32 s4, s98, 1
	s_min_i32 s4, s4, s95
	s_lshl_b32 s5, s4, 18
	s_add_u32 s18, s100, s5
	s_addc_u32 s19, s101, 0
	s_lshl_b32 s5, s98, 18
	s_add_u32 s20, s0, s5
	s_addc_u32 s21, s1, 0
	s_cmp_eq_u32 s4, s95
	s_cbranch_scc1 .Lclamp1p
	global_load_dwordx4 v[8:11], v245, s[18:19]
	global_load_dwordx4 v[4:7], v246, s[18:19]
	global_load_dwordx4 v[130:133], v245, s[20:21]
	global_load_dwordx4 v[12:15], v246, s[20:21]
.Lloads1p_done:
	s_branch .LBB0_20
.LBB0_19:
	s_add_i32 s4, s77, 0x2000
	s_cmpk_lg_i32 s77, 0x4000
	s_cselect_b32 s97, s4, 0
	s_addk_i32 s99, 0x80
	s_cmp_lt_i32 s98, s82
	s_cbranch_scc0 .LBB0_35
.LBB0_20:
	s_add_i32 s83, s66, s98
	s_setprio 1
	ds_read_b64_tr_b16 v[142:143], v234 offset:24576
	ds_read_b64_tr_b16 v[144:145], v234 offset:25088
	v_mfma_f32_32x32x16_f16 v[18:33], v[206:209], v[174:177], v[114:129]
	v_add_f32_e32 v2, v98, v99
	v_add_f32_e32 v2, v100, v2
	v_add_f32_e32 v2, v101, v2
	v_add_f32_e32 v2, v102, v2
	v_add_f32_e32 v2, v103, v2
	v_cvt_pkrtz_f16_f32 v158, v98, v99
	v_cvt_pkrtz_f16_f32 v159, v100, v101
	ds_read_b64_tr_b16 v[138:139], v234 offset:28736
	ds_read_b64_tr_b16 v[140:141], v234 offset:29248
	v_mfma_f32_32x32x16_f16 v[34:49], v[202:205], v[174:177], v[114:129]
	v_add_f32_e32 v2, v104, v2
	v_add_f32_e32 v2, v105, v2
	v_add_f32_e32 v2, v106, v2
	v_add_f32_e32 v2, v107, v2
	v_cvt_pkrtz_f16_f32 v160, v102, v103
	v_cvt_pkrtz_f16_f32 v161, v104, v105
	ds_read_b64_tr_b16 v[134:135], v234 offset:25600
	ds_read_b64_tr_b16 v[136:137], v234 offset:26112
	v_mfma_f32_32x32x16_f16 v[18:33], v[198:201], v[170:173], v[18:33]
	v_add_f32_e32 v2, v108, v2
	v_add_f32_e32 v2, v109, v2
	v_add_f32_e32 v2, v110, v2
	v_add_f32_e32 v2, v111, v2
	v_cvt_pkrtz_f16_f32 v154, v106, v107
	v_cvt_pkrtz_f16_f32 v155, v108, v109
	ds_read_b64_tr_b16 v[106:107], v234 offset:29760
	ds_read_b64_tr_b16 v[108:109], v234 offset:30272
	v_mfma_f32_32x32x16_f16 v[34:49], v[194:197], v[170:173], v[34:49]
	v_add_f32_e32 v2, v112, v2
	v_add_f32_e32 v2, v113, v2
	v_add_f32_e32 v2, v82, v2
	v_add_f32_e32 v2, v83, v2
	v_cvt_pkrtz_f16_f32 v156, v110, v111
	v_cvt_pkrtz_f16_f32 v157, v112, v113
	ds_read_b64_tr_b16 v[102:103], v234 offset:26624
	ds_read_b64_tr_b16 v[104:105], v234 offset:27136
	v_mfma_f32_32x32x16_f16 v[18:33], v[190:193], v[166:169], v[18:33]
	v_add_f32_e32 v2, v84, v2
	v_add_f32_e32 v2, v85, v2
	v_add_f32_e32 v2, v86, v2
	v_add_f32_e32 v2, v87, v2
	v_cvt_pkrtz_f16_f32 v150, v82, v83
	v_cvt_pkrtz_f16_f32 v151, v84, v85
	ds_read_b64_tr_b16 v[98:99], v234 offset:30784
	ds_read_b64_tr_b16 v[100:101], v234 offset:31296
	v_mfma_f32_32x32x16_f16 v[34:49], v[186:189], v[166:169], v[34:49]
	v_add_f32_e32 v2, v88, v2
	v_add_f32_e32 v2, v89, v2
	v_add_f32_e32 v2, v90, v2
	v_add_f32_e32 v2, v91, v2
	v_cvt_pkrtz_f16_f32 v152, v86, v87
	v_cvt_pkrtz_f16_f32 v153, v88, v89
	ds_read_b64_tr_b16 v[86:87], v234 offset:27648
	ds_read_b64_tr_b16 v[88:89], v234 offset:28160
	v_mfma_f32_32x32x16_f16 v[18:33], v[182:185], v[162:165], v[18:33]
	v_add_f32_e32 v2, v92, v2
	v_add_f32_e32 v2, v93, v2
	v_add_f32_e32 v2, v94, v2
	v_add_f32_e32 v2, v95, v2
	v_cvt_pkrtz_f16_f32 v146, v90, v91
	v_cvt_pkrtz_f16_f32 v147, v92, v93
	ds_read_b64_tr_b16 v[82:83], v234 offset:31808
	ds_read_b64_tr_b16 v[84:85], v234 offset:32320
	v_mfma_f32_32x32x16_f16 v[34:49], v[178:181], v[162:165], v[34:49]
	v_add_f32_e32 v2, v96, v2
	v_add_f32_e32 v2, v97, v2
	v_add_f32_e32 v2, 0, v2
	v_cvt_pkrtz_f16_f32 v148, v94, v95
	v_cvt_pkrtz_f16_f32 v149, v96, v97
	s_setprio 0
	s_cmp_lg_u32 s83, 0
	s_cselect_b64 s[4:5], -1, 0
	s_or_b64 s[4:5], s[4:5], s[80:81]
	s_and_b64 vcc, exec, s[4:5]
	s_cbranch_vccnz .LBB0_22
	v_mov_b32_e32 v16, v229
	s_nop 0
	v_ashrrev_i32_e32 v16, 3, v16
	v_and_b32_e32 v16, -4, v16
	v_add_u32_e32 v16, s99, v16
	v_add_u32_e32 v17, 0xffffff85, v16
	v_cmp_gt_i32_e64 s[26:27], s3, v17
	v_add_u32_e32 v17, 0xffffffa5, v16
	v_cmp_gt_i32_e32 vcc, s3, v17
	v_add_u32_e32 v17, 0xffffff86, v16
	v_cmp_gt_i32_e64 s[30:31], s3, v17
	v_add_u32_e32 v17, 0xffffffa6, v16
	v_cmp_gt_i32_e64 s[40:41], s3, v17
	v_add_u32_e32 v17, 0xffffff87, v16
	v_cmp_gt_i32_e64 s[36:37], s3, v17
	v_add_u32_e32 v17, 0xffffffa7, v16
	v_cmp_gt_i32_e64 s[4:5], s3, v17
	v_add_u32_e32 v17, 0xffffff88, v16
	v_cmp_gt_i32_e64 s[38:39], s3, v17
	v_add_u32_e32 v17, 0xffffffa8, v16
	v_cmp_gt_i32_e64 s[6:7], s3, v17
	v_add_u32_e32 v17, 0xffffff8d, v16
	v_cmp_gt_i32_e64 s[42:43], s3, v17
	v_add_u32_e32 v17, 0xffffffad, v16
	v_cmp_gt_i32_e64 s[8:9], s3, v17
	v_add_u32_e32 v17, 0xffffff8e, v16
	v_cmp_gt_i32_e64 s[44:45], s3, v17
	v_add_u32_e32 v17, 0xffffffae, v16
	v_cmp_gt_i32_e64 s[10:11], s3, v17
	v_add_u32_e32 v17, 0xffffff8f, v16
	v_cmp_gt_i32_e64 s[46:47], s3, v17
	v_add_u32_e32 v17, 0xffffffaf, v16
	v_cmp_gt_i32_e64 s[12:13], s3, v17
	v_add_u32_e32 v17, 0xffffff90, v16
	v_cmp_gt_i32_e64 s[48:49], s3, v17
	v_add_u32_e32 v17, 0xffffffb0, v16
	v_cmp_gt_i32_e64 s[14:15], s3, v17
	v_add_u32_e32 v17, 0xffffff95, v16
	v_cmp_gt_i32_e64 s[50:51], s3, v17
	v_add_u32_e32 v17, 0xffffffb5, v16
	v_cmp_gt_i32_e64 s[16:17], s3, v17
	v_add_u32_e32 v17, 0xffffff96, v16
	v_cmp_gt_i32_e64 s[52:53], s3, v17
	v_add_u32_e32 v17, 0xffffffb6, v16
	v_cmp_gt_i32_e64 s[18:19], s3, v17
	v_add_u32_e32 v17, 0xffffff97, v16
	v_cmp_gt_i32_e64 s[54:55], s3, v17
	v_add_u32_e32 v17, 0xffffffb7, v16
	v_cmp_gt_i32_e64 s[20:21], s3, v17
	v_add_u32_e32 v17, 0xffffff98, v16
	v_cmp_gt_i32_e64 s[56:57], s3, v17
	v_add_u32_e32 v17, 0xffffffb8, v16
	v_cmp_gt_i32_e64 s[22:23], s3, v17
	v_add_u32_e32 v17, 0xffffff9d, v16
	v_cmp_gt_i32_e64 s[58:59], s3, v17
	v_add_u32_e32 v17, 0xffffffbd, v16
	v_cmp_gt_i32_e64 s[24:25], s3, v17
	v_add_u32_e32 v17, 0xffffff9e, v16
	v_cmp_gt_i32_e64 s[60:61], s3, v17
	v_add_u32_e32 v17, 0xffffffbe, v16
	v_cmp_gt_i32_e64 s[28:29], s3, v17
	v_add_u32_e32 v17, 0xffffff9f, v16
	v_cmp_gt_i32_e64 s[62:63], s3, v17
	v_add_u32_e32 v17, 0xffffffbf, v16
	v_cmp_gt_i32_e64 s[34:35], s3, v17
	v_add_u32_e32 v17, 0xffffffa0, v16
	v_cmp_gt_i32_e64 s[64:65], s3, v17
	s_or_b64 s[62:63], s[64:65], s[62:63]
	s_or_b64 s[60:61], s[62:63], s[60:61]
	s_or_b64 s[58:59], s[60:61], s[58:59]
	s_or_b64 s[56:57], s[58:59], s[56:57]
	s_or_b64 s[54:55], s[56:57], s[54:55]
	s_or_b64 s[52:53], s[54:55], s[52:53]
	s_or_b64 s[50:51], s[52:53], s[50:51]
	s_or_b64 s[48:49], s[50:51], s[48:49]
	s_or_b64 s[46:47], s[48:49], s[46:47]
	s_or_b64 s[44:45], s[46:47], s[44:45]
	s_or_b64 s[42:43], s[44:45], s[42:43]
	s_or_b64 s[38:39], s[42:43], s[38:39]
	s_or_b64 s[36:37], s[38:39], s[36:37]
	s_or_b64 s[30:31], s[36:37], s[30:31]
	s_or_b64 s[26:27], s[30:31], s[26:27]
	v_subrev_u32_e32 v16, 64, v16
	v_cndmask_b32_e64 v18, v242, v18, s[26:27]
	v_cmp_gt_i32_e64 s[26:27], s3, v16
	v_cndmask_b32_e64 v33, v242, v33, s[64:65]
	v_cndmask_b32_e64 v32, v242, v32, s[62:63]
	v_cndmask_b32_e64 v49, v242, v49, s[26:27]
	s_or_b64 s[26:27], s[26:27], s[34:35]
	v_cndmask_b32_e64 v48, v242, v48, s[26:27]
	s_or_b64 s[26:27], s[26:27], s[28:29]
	s_or_b64 s[24:25], s[26:27], s[24:25]
	s_or_b64 s[22:23], s[24:25], s[22:23]
	s_or_b64 s[20:21], s[22:23], s[20:21]
	s_or_b64 s[18:19], s[20:21], s[18:19]
	s_or_b64 s[16:17], s[18:19], s[16:17]
	s_or_b64 s[14:15], s[16:17], s[14:15]
	s_or_b64 s[12:13], s[14:15], s[12:13]
	s_or_b64 s[10:11], s[12:13], s[10:11]
	s_or_b64 s[8:9], s[10:11], s[8:9]
	s_or_b64 s[6:7], s[8:9], s[6:7]
	s_or_b64 s[4:5], s[6:7], s[4:5]
	v_cndmask_b32_e64 v36, v242, v36, s[4:5]
	s_or_b64 s[4:5], s[4:5], s[40:41]
	s_or_b64 vcc, s[4:5], vcc
	v_cndmask_b32_e64 v31, v242, v31, s[60:61]
	v_cndmask_b32_e64 v30, v242, v30, s[58:59]
	v_cndmask_b32_e64 v29, v242, v29, s[56:57]
	v_cndmask_b32_e64 v28, v242, v28, s[54:55]
	v_cndmask_b32_e64 v27, v242, v27, s[52:53]
	v_cndmask_b32_e64 v26, v242, v26, s[50:51]
	v_cndmask_b32_e64 v25, v242, v25, s[48:49]
	v_cndmask_b32_e64 v24, v242, v24, s[46:47]
	v_cndmask_b32_e64 v23, v242, v23, s[44:45]
	v_cndmask_b32_e64 v22, v242, v22, s[42:43]
	v_cndmask_b32_e64 v21, v242, v21, s[38:39]
	v_cndmask_b32_e64 v20, v242, v20, s[36:37]
	v_cndmask_b32_e64 v19, v242, v19, s[30:31]
	v_cndmask_b32_e64 v47, v242, v47, s[26:27]
	v_cndmask_b32_e64 v46, v242, v46, s[24:25]
	v_cndmask_b32_e64 v45, v242, v45, s[22:23]
	v_cndmask_b32_e64 v44, v242, v44, s[20:21]
	v_cndmask_b32_e64 v43, v242, v43, s[18:19]
	v_cndmask_b32_e64 v42, v242, v42, s[16:17]
	v_cndmask_b32_e64 v41, v242, v41, s[14:15]
	v_cndmask_b32_e64 v40, v242, v40, s[12:13]
	v_cndmask_b32_e64 v39, v242, v39, s[10:11]
	v_cndmask_b32_e64 v38, v242, v38, s[8:9]
	v_cndmask_b32_e64 v37, v242, v37, s[6:7]
	v_cndmask_b32_e64 v35, v242, v35, s[4:5]
	v_cndmask_b32_e32 v34, v242, v34, vcc

.LBB0_30:
	s_add_i32 s6, s97, 0x2000
	s_cmpk_lg_i32 s97, 0x4000
	s_cselect_b32 s77, s6, 0
	s_setprio 1
	s_waitcnt lgkmcnt(14)
	v_mfma_f32_32x32x16_f16 v[50:65], v[194:197], v[158:161], v[50:65]
	v_exp_f32_e32 v98, v98
	v_exp_f32_e32 v99, v99
	v_exp_f32_e32 v100, v100
	v_exp_f32_e32 v101, v101
	s_waitcnt lgkmcnt(12)
	v_mfma_f32_32x32x16_f16 v[66:81], v[190:193], v[158:161], v[66:81]
	v_exp_f32_e32 v102, v102
	v_exp_f32_e32 v103, v103
	v_exp_f32_e32 v104, v104
	v_exp_f32_e32 v105, v105
	v_add_u32_e32 v2, s97, v230
	ds_read_b128 v[206:209], v2
	ds_read_b128 v[202:205], v2 offset:4096
	s_waitcnt lgkmcnt(12)
	v_mfma_f32_32x32x16_f16 v[50:65], v[186:189], v[154:157], v[50:65]
	v_exp_f32_e32 v106, v106
	v_exp_f32_e32 v107, v107
	v_exp_f32_e32 v108, v108
	v_exp_f32_e32 v109, v109
	v_add_u32_e32 v2, s97, v231
	ds_read_b128 v[198:201], v2
	ds_read_b128 v[194:197], v2 offset:4096
	s_waitcnt lgkmcnt(12)
	v_mfma_f32_32x32x16_f16 v[66:81], v[182:185], v[154:157], v[66:81]
	v_exp_f32_e32 v110, v110
	v_exp_f32_e32 v111, v111
	v_exp_f32_e32 v112, v112
	v_exp_f32_e32 v113, v113
	v_add_u32_e32 v2, s97, v232
	ds_read_b128 v[190:193], v2
	ds_read_b128 v[186:189], v2 offset:4096
	s_waitcnt lgkmcnt(12)
	v_mfma_f32_32x32x16_f16 v[50:65], v[178:181], v[150:153], v[50:65]
	v_exp_f32_e32 v82, v82
	v_exp_f32_e32 v83, v83
	v_exp_f32_e32 v84, v84
	v_exp_f32_e32 v85, v85
	v_add_u32_e32 v2, s97, v233
	ds_read_b128 v[182:185], v2
	ds_read_b128 v[178:181], v2 offset:4096
	s_waitcnt lgkmcnt(12)
	v_mfma_f32_32x32x16_f16 v[66:81], v[222:225], v[150:153], v[66:81]
	v_exp_f32_e32 v86, v86
	v_exp_f32_e32 v87, v87
	v_exp_f32_e32 v88, v88
	v_exp_f32_e32 v89, v89
	s_waitcnt lgkmcnt(10)
	v_mfma_f32_32x32x16_f16 v[50:65], v[218:221], v[146:149], v[50:65]
	v_exp_f32_e32 v90, v90
	v_exp_f32_e32 v91, v91
	v_exp_f32_e32 v92, v92
	v_exp_f32_e32 v93, v93
	s_waitcnt lgkmcnt(8)
	v_mfma_f32_32x32x16_f16 v[66:81], v[214:217], v[146:149], v[66:81]
	v_exp_f32_e32 v94, v94
	v_exp_f32_e32 v95, v95
	v_exp_f32_e32 v96, v96
	v_exp_f32_e32 v97, v97
	s_setprio 0
	s_waitcnt vmcnt(3)
	v_cvt_pkrtz_f16_f32 v8, v8, v9
	v_cvt_pkrtz_f16_f32 v9, v10, v11
	v_add_u32_e32 v17, s77, v249
	s_waitcnt vmcnt(2)
	v_cvt_pkrtz_f16_f32 v4, v4, v5
	v_cvt_pkrtz_f16_f32 v5, v6, v7
	ds_write2st64_b64 v17, v[8:9], v[4:5] offset1:8
	s_waitcnt vmcnt(1)
	v_cvt_pkrtz_f16_f32 v146, v210, v211
	v_cvt_pkrtz_f16_f32 v147, v212, v213
	s_waitcnt vmcnt(0)
	v_cvt_pkrtz_f16_f32 v16, v12, v13
	v_cvt_pkrtz_f16_f32 v17, v14, v15
	s_andn2_b64 vcc, exec, s[4:5]
	ds_write2st64_b64 v251, v[146:147], v[16:17] offset0:48 offset1:52
	s_cmp_lt_i32 s98, s82
	s_cbranch_scc0 .Lloads1e_done
	s_add_i32 s4, s98, 1
	s_min_i32 s4, s4, s95
	s_lshl_b32 s5, s4, 18
	s_add_u32 s18, s100, s5
	s_addc_u32 s19, s101, 0
	s_lshl_b32 s5, s98, 18
	s_add_u32 s20, s0, s5
	s_addc_u32 s21, s1, 0
	s_cmp_eq_u32 s4, s95
	s_cbranch_scc1 .Lclamp1e
	global_load_dwordx4 v[8:11], v245, s[18:19]
	global_load_dwordx4 v[4:7], v246, s[18:19]
	global_load_dwordx4 v[130:133], v245, s[20:21]
	global_load_dwordx4 v[12:15], v246, s[20:21]
.Lloads1e_done:
	s_waitcnt lgkmcnt(0)
	s_barrier
	s_cbranch_vccnz .LBB0_19
	v_pk_mul_f32 v[64:65], v[228:229], v[64:65] op_sel_hi:[0,1]
	v_pk_mul_f32 v[62:63], v[228:229], v[62:63] op_sel_hi:[0,1]
	v_pk_mul_f32 v[60:61], v[228:229], v[60:61] op_sel_hi:[0,1]
	v_pk_mul_f32 v[58:59], v[228:229], v[58:59] op_sel_hi:[0,1]
	v_pk_mul_f32 v[56:57], v[228:229], v[56:57] op_sel_hi:[0,1]
	v_pk_mul_f32 v[54:55], v[228:229], v[54:55] op_sel_hi:[0,1]
	v_pk_mul_f32 v[52:53], v[228:229], v[52:53] op_sel_hi:[0,1]
	v_pk_mul_f32 v[50:51], v[228:229], v[50:51] op_sel_hi:[0,1]
	v_pk_mul_f32 v[80:81], v[228:229], v[80:81] op_sel_hi:[0,1]
	v_pk_mul_f32 v[78:79], v[228:229], v[78:79] op_sel_hi:[0,1]
	v_pk_mul_f32 v[76:77], v[228:229], v[76:77] op_sel_hi:[0,1]
	v_pk_mul_f32 v[74:75], v[228:229], v[74:75] op_sel_hi:[0,1]
	v_pk_mul_f32 v[72:73], v[228:229], v[72:73] op_sel_hi:[0,1]
	v_pk_mul_f32 v[70:71], v[228:229], v[70:71] op_sel_hi:[0,1]
	v_pk_mul_f32 v[68:69], v[228:229], v[68:69] op_sel_hi:[0,1]
	v_pk_mul_f32 v[66:67], v[228:229], v[66:67] op_sel_hi:[0,1]
	s_branch .LBB0_19

.Lclamp1e:
	s_lshl_b32 s5, s4, 6
	s_sub_i32 s5, s96, s5
	v_lshrrev_b32_e32 v148, 4, v0
	v_and_b32_e32 v149, 15, v0
	v_lshlrev_b32_e32 v149, 4, v149
	v_min_i32_e32 v150, s5, v148
	v_lshl_add_u32 v150, v150, 12, v149
	global_load_dwordx4 v[8:11], v150, s[18:19]
	v_add_u32_e32 v150, 32, v148
	v_min_i32_e32 v150, s5, v150
	v_lshl_add_u32 v150, v150, 12, v149
	global_load_dwordx4 v[4:7], v150, s[18:19]
	s_lshl_b32 s5, s98, 6
	s_sub_i32 s5, s96, s5
	s_add_i32 s5, s5, 64
	v_min_i32_e32 v150, s5, v148
	v_lshl_add_u32 v150, v150, 12, v149
	global_load_dwordx4 v[130:133], v150, s[20:21]
	v_add_u32_e32 v150, 32, v148
	v_min_i32_e32 v150, s5, v150
	v_lshl_add_u32 v150, v150, 12, v149
	global_load_dwordx4 v[12:15], v150, s[20:21]
	s_branch .Lloads1e_done
